# baseline (speedup 1.0000x reference)
.Lg_s3skip0:
	s_cmp_eq_u32 s10, 10
	s_cselect_b32 s32, s46, s32
	s_sub_u32 s18, s10, 4
	s_cmp_lt_u32 s18, s9
	s_cselect_b32 s19, s32, 0x80000000
	ds_read_b128 v[226:229], v245 offset:0
	s_add_u32 s32, s32, 0x40000
	v_readlane_b32 s13, v247, s18
	v_lshrrev_b32_e32 v249, 4, v1
	v_lshlrev_b32_e32 v249, 3, v249
	v_lshrrev_b32_e64 v249, v249, s13
	v_and_b32_e32 v249, 0xff, v249
	v_cmp_eq_u32_e32 vcc, 1, v249
	s_nop 1
	v_cndmask_b32_e32 v249, v255, v246, vcc
	s_waitcnt lgkmcnt(0)
	s_cmp_ge_u32 s10, 9
	s_cbranch_scc1 .Lg_s4late0
	buffer_store_dwordx4 v[226:229], v249, s[28:31], s19 offen sc0 sc1
	s_branch .Lg_s4done0
.Lg_s4late0:
	buffer_store_dwordx4 v[226:229], v249, s[28:31], s19 offen nt

.Lg_s3skip1:
	s_cmp_eq_u32 s10, 10
	s_cselect_b32 s32, s46, s32
	s_sub_u32 s18, s10, 4
	s_cmp_lt_u32 s18, s9
	s_cselect_b32 s19, s32, 0x80000000
	ds_read_b128 v[226:229], v245 offset:4352
	s_add_u32 s32, s32, 0x40000
	v_readlane_b32 s13, v247, s18
	v_lshrrev_b32_e32 v249, 4, v1
	v_lshlrev_b32_e32 v249, 3, v249
	v_lshrrev_b32_e64 v249, v249, s13
	v_and_b32_e32 v249, 0xff, v249
	v_cmp_eq_u32_e32 vcc, 1, v249
	s_nop 1
	v_cndmask_b32_e32 v249, v255, v246, vcc
	s_waitcnt lgkmcnt(0)
	s_cmp_ge_u32 s10, 9
	s_cbranch_scc1 .Lg_s4late1
	buffer_store_dwordx4 v[226:229], v249, s[28:31], s19 offen sc0 sc1
	s_branch .Lg_s4done1
